# v22: v16 + software-pipelined LDS table set-up loops (router x2, gate columns, combine3/4 tables): all loads issued first, counted waits
# speedup vs baseline: 1.0071x; 1.0014x over previous
.LBB0_135:
	global_load_dwordx4 v[168:171], v[0:1], off
	global_load_dwordx4 v[172:175], v[0:1], off offset:16
	v_lshl_add_u64 v[0:1], v[0:1], 0, s[10:11]
	global_load_dwordx4 v[176:179], v[0:1], off
	global_load_dwordx4 v[180:183], v[0:1], off offset:16
	v_lshl_add_u64 v[0:1], v[0:1], 0, s[10:11]
	global_load_dwordx4 v[184:187], v[0:1], off
	global_load_dwordx4 v[188:191], v[0:1], off offset:16
	v_lshl_add_u64 v[0:1], v[0:1], 0, s[10:11]
	global_load_dwordx4 v[4:7], v[0:1], off
	global_load_dwordx4 v[8:11], v[0:1], off offset:16
	v_lshl_add_u64 v[0:1], v[0:1], 0, s[10:11]
	v_add_u32_e32 v2, 0x800, v2
	s_waitcnt vmcnt(7)
	ds_write2st64_b32 v3, v168, v169 offset1:32
	s_waitcnt vmcnt(6)
	ds_write2st64_b32 v3, v172, v173 offset0:128 offset1:160
	ds_write2st64_b32 v3, v170, v171 offset0:64 offset1:96
	ds_write2st64_b32 v3, v174, v175 offset0:192 offset1:224
	s_waitcnt vmcnt(5)
	ds_write2st64_b32 v3, v176, v177 offset0:8 offset1:40
	s_waitcnt vmcnt(4)
	ds_write2st64_b32 v3, v180, v181 offset0:136 offset1:168
	ds_write2st64_b32 v3, v178, v179 offset0:72 offset1:104
	ds_write2st64_b32 v3, v182, v183 offset0:200 offset1:232
	s_waitcnt vmcnt(3)
	ds_write2st64_b32 v3, v184, v185 offset0:16 offset1:48
	s_waitcnt vmcnt(2)
	ds_write2st64_b32 v3, v188, v189 offset0:144 offset1:176
	ds_write2st64_b32 v3, v186, v187 offset0:80 offset1:112
	ds_write2st64_b32 v3, v190, v191 offset0:208 offset1:240
	s_waitcnt vmcnt(1)
	ds_write2st64_b32 v3, v4, v5 offset0:24 offset1:56
	s_waitcnt vmcnt(0)
	ds_write2st64_b32 v3, v8, v9 offset0:152 offset1:184
	ds_write2st64_b32 v3, v6, v7 offset0:88 offset1:120
	ds_write2st64_b32 v3, v10, v11 offset0:216 offset1:248
	v_add_u32_e32 v3, 0x2000, v3

.LBB0_1566:
	s_waitcnt lgkmcnt(0)
	v_lshlrev_b32_e32 v0, 6, v3
	v_lshl_add_u64 v[4:5], s[6:7], 0, v[0:1]
	s_add_u32 s98, s6, 0x8000
	s_addc_u32 s99, s7, 0
	v_lshl_add_u64 v[6:7], s[98:99], 0, v[0:1]
	s_add_u32 s98, s6, 0x10000
	s_addc_u32 s99, s7, 0
	v_lshl_add_u64 v[8:9], s[98:99], 0, v[0:1]
	s_add_u32 s98, s6, 0x18000
	s_addc_u32 s99, s7, 0
	v_lshl_add_u64 v[10:11], s[98:99], 0, v[0:1]
	global_load_dwordx4 v[168:171], v[4:5], off
	global_load_dwordx4 v[172:175], v[6:7], off
	global_load_dwordx4 v[176:179], v[8:9], off
	global_load_dwordx4 v[180:183], v[10:11], off
	global_load_dwordx4 v[184:187], v[4:5], off offset:16
	global_load_dwordx4 v[188:191], v[6:7], off offset:16
	global_load_dwordx4 v[192:195], v[8:9], off offset:16
	global_load_dwordx4 v[196:199], v[10:11], off offset:16
	global_load_dwordx4 v[200:203], v[4:5], off offset:32
	global_load_dwordx4 v[220:223], v[6:7], off offset:32
	global_load_dwordx4 v[224:227], v[8:9], off offset:32
	global_load_dwordx4 v[228:231], v[10:11], off offset:32
	global_load_dwordx4 v[232:235], v[4:5], off offset:48
	global_load_dwordx4 v[236:239], v[6:7], off offset:48
	global_load_dwordx4 v[240:243], v[8:9], off offset:48
	global_load_dwordx4 v[244:247], v[10:11], off offset:48
	v_lshlrev_b32_e32 v0, 2, v3
	v_add_u32_e32 v3, 0x10000, v0
	s_waitcnt vmcnt(15)
	ds_write2st64_b32 v0, v168, v169 offset1:32
	ds_write2st64_b32 v0, v170, v171 offset0:64 offset1:96
	s_waitcnt vmcnt(14)
	ds_write2st64_b32 v0, v172, v173 offset0:8 offset1:40
	ds_write2st64_b32 v0, v174, v175 offset0:72 offset1:104
	s_waitcnt vmcnt(13)
	ds_write2st64_b32 v0, v176, v177 offset0:16 offset1:48
	ds_write2st64_b32 v0, v178, v179 offset0:80 offset1:112
	s_waitcnt vmcnt(12)
	ds_write2st64_b32 v0, v180, v181 offset0:24 offset1:56
	ds_write2st64_b32 v0, v182, v183 offset0:88 offset1:120
	s_waitcnt vmcnt(11)
	ds_write2st64_b32 v0, v184, v185 offset0:128 offset1:160
	ds_write2st64_b32 v0, v186, v187 offset0:192 offset1:224
	s_waitcnt vmcnt(10)
	ds_write2st64_b32 v0, v188, v189 offset0:136 offset1:168
	ds_write2st64_b32 v0, v190, v191 offset0:200 offset1:232
	s_waitcnt vmcnt(9)
	ds_write2st64_b32 v0, v192, v193 offset0:144 offset1:176
	ds_write2st64_b32 v0, v194, v195 offset0:208 offset1:240
	s_waitcnt vmcnt(8)
	ds_write2st64_b32 v0, v196, v197 offset0:152 offset1:184
	ds_write2st64_b32 v0, v198, v199 offset0:216 offset1:248
	s_waitcnt vmcnt(7)
	ds_write2st64_b32 v3, v200, v201 offset1:32
	ds_write2st64_b32 v3, v202, v203 offset0:64 offset1:96
	s_waitcnt vmcnt(6)
	ds_write2st64_b32 v3, v220, v221 offset0:8 offset1:40
	ds_write2st64_b32 v3, v222, v223 offset0:72 offset1:104
	s_waitcnt vmcnt(5)
	ds_write2st64_b32 v3, v224, v225 offset0:16 offset1:48
	ds_write2st64_b32 v3, v226, v227 offset0:80 offset1:112
	s_waitcnt vmcnt(4)
	ds_write2st64_b32 v3, v228, v229 offset0:24 offset1:56
	ds_write2st64_b32 v3, v230, v231 offset0:88 offset1:120
	s_waitcnt vmcnt(3)
	ds_write2st64_b32 v3, v232, v233 offset0:128 offset1:160
	ds_write2st64_b32 v3, v234, v235 offset0:192 offset1:224
	s_waitcnt vmcnt(2)
	ds_write2st64_b32 v3, v236, v237 offset0:136 offset1:168
	ds_write2st64_b32 v3, v238, v239 offset0:200 offset1:232
	s_waitcnt vmcnt(1)
	ds_write2st64_b32 v3, v240, v241 offset0:144 offset1:176
	ds_write2st64_b32 v3, v242, v243 offset0:208 offset1:240
	s_waitcnt vmcnt(0)
	ds_write2st64_b32 v3, v244, v245 offset0:152 offset1:184
	ds_write2st64_b32 v3, v246, v247 offset0:216 offset1:248

.LBB0_1728:
	s_waitcnt lgkmcnt(0)
	v_lshlrev_b32_e32 v0, 6, v3
	v_lshl_add_u64 v[4:5], s[8:9], 0, v[0:1]
	s_add_u32 s98, s8, 0x8000
	s_addc_u32 s99, s9, 0
	v_lshl_add_u64 v[6:7], s[98:99], 0, v[0:1]
	s_add_u32 s98, s8, 0x10000
	s_addc_u32 s99, s9, 0
	v_lshl_add_u64 v[8:9], s[98:99], 0, v[0:1]
	s_add_u32 s98, s8, 0x18000
	s_addc_u32 s99, s9, 0
	v_lshl_add_u64 v[10:11], s[98:99], 0, v[0:1]
	global_load_dwordx4 v[168:171], v[4:5], off
	global_load_dwordx4 v[172:175], v[6:7], off
	global_load_dwordx4 v[176:179], v[8:9], off
	global_load_dwordx4 v[180:183], v[10:11], off
	global_load_dwordx4 v[184:187], v[4:5], off offset:16
	global_load_dwordx4 v[188:191], v[6:7], off offset:16
	global_load_dwordx4 v[192:195], v[8:9], off offset:16
	global_load_dwordx4 v[196:199], v[10:11], off offset:16
	global_load_dwordx4 v[200:203], v[4:5], off offset:32
	global_load_dwordx4 v[220:223], v[6:7], off offset:32
	global_load_dwordx4 v[224:227], v[8:9], off offset:32
	global_load_dwordx4 v[228:231], v[10:11], off offset:32
	global_load_dwordx4 v[232:235], v[4:5], off offset:48
	global_load_dwordx4 v[236:239], v[6:7], off offset:48
	global_load_dwordx4 v[240:243], v[8:9], off offset:48
	global_load_dwordx4 v[244:247], v[10:11], off offset:48
	v_lshlrev_b32_e32 v0, 2, v3
	v_add_u32_e32 v3, 0x10000, v0
	s_waitcnt vmcnt(15)
	ds_write2st64_b32 v0, v168, v169 offset1:32
	ds_write2st64_b32 v0, v170, v171 offset0:64 offset1:96
	s_waitcnt vmcnt(14)
	ds_write2st64_b32 v0, v172, v173 offset0:8 offset1:40
	ds_write2st64_b32 v0, v174, v175 offset0:72 offset1:104
	s_waitcnt vmcnt(13)
	ds_write2st64_b32 v0, v176, v177 offset0:16 offset1:48
	ds_write2st64_b32 v0, v178, v179 offset0:80 offset1:112
	s_waitcnt vmcnt(12)
	ds_write2st64_b32 v0, v180, v181 offset0:24 offset1:56
	ds_write2st64_b32 v0, v182, v183 offset0:88 offset1:120
	s_waitcnt vmcnt(11)
	ds_write2st64_b32 v0, v184, v185 offset0:128 offset1:160
	ds_write2st64_b32 v0, v186, v187 offset0:192 offset1:224
	s_waitcnt vmcnt(10)
	ds_write2st64_b32 v0, v188, v189 offset0:136 offset1:168
	ds_write2st64_b32 v0, v190, v191 offset0:200 offset1:232
	s_waitcnt vmcnt(9)
	ds_write2st64_b32 v0, v192, v193 offset0:144 offset1:176
	ds_write2st64_b32 v0, v194, v195 offset0:208 offset1:240
	s_waitcnt vmcnt(8)
	ds_write2st64_b32 v0, v196, v197 offset0:152 offset1:184
	ds_write2st64_b32 v0, v198, v199 offset0:216 offset1:248
	s_waitcnt vmcnt(7)
	ds_write2st64_b32 v3, v200, v201 offset1:32
	ds_write2st64_b32 v3, v202, v203 offset0:64 offset1:96
	s_waitcnt vmcnt(6)
	ds_write2st64_b32 v3, v220, v221 offset0:8 offset1:40
	ds_write2st64_b32 v3, v222, v223 offset0:72 offset1:104
	s_waitcnt vmcnt(5)
	ds_write2st64_b32 v3, v224, v225 offset0:16 offset1:48
	ds_write2st64_b32 v3, v226, v227 offset0:80 offset1:112
	s_waitcnt vmcnt(4)
	ds_write2st64_b32 v3, v228, v229 offset0:24 offset1:56
	ds_write2st64_b32 v3, v230, v231 offset0:88 offset1:120
	s_waitcnt vmcnt(3)
	ds_write2st64_b32 v3, v232, v233 offset0:128 offset1:160
	ds_write2st64_b32 v3, v234, v235 offset0:192 offset1:224
	s_waitcnt vmcnt(2)
	ds_write2st64_b32 v3, v236, v237 offset0:136 offset1:168
	ds_write2st64_b32 v3, v238, v239 offset0:200 offset1:232
	s_waitcnt vmcnt(1)
	ds_write2st64_b32 v3, v240, v241 offset0:144 offset1:176
	ds_write2st64_b32 v3, v242, v243 offset0:208 offset1:240
	s_waitcnt vmcnt(0)
	ds_write2st64_b32 v3, v244, v245 offset0:152 offset1:184
	ds_write2st64_b32 v3, v246, v247 offset0:216 offset1:248

.LBB0_3117:
	s_or_b64 exec, exec, s[8:9]
	v_add_u32_e32 v6, s0, v0
	s_movk_i32 s0, 0x1800
	v_cmp_gt_i32_e32 vcc, s0, v6
	s_waitcnt lgkmcnt(0)
	s_barrier
	s_and_saveexec_b64 s[8:9], vcc
	s_cbranch_execz .LBB0_3128
	v_readlane_b32 s0, v252, 3
	v_readlane_b32 s1, v252, 4
	s_load_dwordx2 s[0:1], s[0:1], 0x20
	v_lshlrev_b32_e32 v1, 4, v0
	v_lshlrev_b32_e32 v0, 2, v0
	v_readlane_b32 s10, v252, 10
	s_mov_b64 s[16:17], 0
	v_mov_b32_e32 v5, 0
	v_lshl_add_u32 v7, s10, 10, v1
	v_lshl_add_u32 v8, s10, 8, v0
	s_waitcnt lgkmcnt(0)
	s_add_u32 s10, s0, 0x2000
	s_addc_u32 s11, s1, 0
	s_add_u32 s12, s4, 0x12000
	s_addc_u32 s13, s5, 0
	s_add_u32 s14, s4, 0x38000
	s_addc_u32 s15, s5, 0
	s_mov_b32 s0, 0xc000
	s_movk_i32 s1, 0x15ff
	v_lshrrev_b32_e32 v164, 4, v6
	v_and_b32_e32 v0, 0x400, v8
	v_and_b32_e32 v1, 0x3f0, v7
	v_and_b32_e32 v164, 12, v164
	v_or3_b32 v164, v0, v1, v164
	v_lshlrev_b32_e32 v164, 2, v164
	s_mov_b64 s[98:99], s[12:13]
	global_load_dwordx4 v[168:171], v164, s[98:99]
	s_add_u32 s98, s12, 0xc000
	s_addc_u32 s99, s13, 0
	global_load_dwordx4 v[172:175], v164, s[98:99]
	s_add_u32 s98, s12, 0x18000
	s_addc_u32 s99, s13, 0
	global_load_dwordx4 v[176:179], v164, s[98:99]
	s_add_u32 s98, s12, 0x24000
	s_addc_u32 s99, s13, 0
	global_load_dwordx4 v[180:183], v164, s[98:99]
	global_load_dwordx4 v[184:187], v164, s[10:11]
	s_add_u32 s98, s14, 0x2000
	s_addc_u32 s99, s15, 0
	global_load_dwordx4 v[188:191], v164, s[98:99]
	s_add_u32 s98, s14, 0xe000
	s_addc_u32 s99, s15, 0
	global_load_dwordx4 v[192:195], v164, s[98:99]
	s_add_u32 s98, s14, 0x1a000
	s_addc_u32 s99, s15, 0
	global_load_dwordx4 v[196:199], v164, s[98:99]
	s_add_u32 s98, s14, 0x26000
	s_addc_u32 s99, s15, 0
	global_load_dwordx4 v[200:203], v164, s[98:99]
	s_mov_b64 s[98:99], s[14:15]
	global_load_dwordx4 v[220:223], v164, s[98:99]
	s_add_u32 s98, s14, 0xc000
	s_addc_u32 s99, s15, 0
	global_load_dwordx4 v[224:227], v164, s[98:99]
	s_add_u32 s98, s14, 0x18000
	s_addc_u32 s99, s15, 0
	global_load_dwordx4 v[228:231], v164, s[98:99]
	s_add_u32 s98, s14, 0x24000
	s_addc_u32 s99, s15, 0
	global_load_dwordx4 v[232:235], v164, s[98:99]
	v_add_u32_e32 v165, 0x10000, v7
	s_waitcnt vmcnt(12)
	ds_write_b128 v7, v[168:171]
	s_waitcnt vmcnt(11)
	ds_write_b128 v7, v[172:175] offset:8192
	s_waitcnt vmcnt(10)
	ds_write_b128 v7, v[176:179] offset:16384
	s_waitcnt vmcnt(9)
	ds_write_b128 v7, v[180:183] offset:24576
	s_waitcnt vmcnt(7)
	v_pk_add_f32 v[190:191], v[190:191], 1.0 op_sel_hi:[1,0]
	v_pk_add_f32 v[188:189], v[188:189], 1.0 op_sel_hi:[1,0]
	v_pk_mul_f32 v[190:191], v[186:187], v[190:191]
	v_pk_mul_f32 v[188:189], v[184:185], v[188:189]
	ds_write_b128 v7, v[188:191] offset:32768
	s_waitcnt vmcnt(6)
	v_pk_add_f32 v[194:195], v[194:195], 1.0 op_sel_hi:[1,0]
	v_pk_add_f32 v[192:193], v[192:193], 1.0 op_sel_hi:[1,0]
	v_pk_mul_f32 v[194:195], v[186:187], v[194:195]
	v_pk_mul_f32 v[192:193], v[184:185], v[192:193]
	ds_write_b128 v7, v[192:195] offset:40960
	s_waitcnt vmcnt(5)
	v_pk_add_f32 v[198:199], v[198:199], 1.0 op_sel_hi:[1,0]
	v_pk_add_f32 v[196:197], v[196:197], 1.0 op_sel_hi:[1,0]
	v_pk_mul_f32 v[198:199], v[186:187], v[198:199]
	v_pk_mul_f32 v[196:197], v[184:185], v[196:197]
	ds_write_b128 v7, v[196:199] offset:49152
	s_waitcnt vmcnt(4)
	v_pk_add_f32 v[202:203], v[202:203], 1.0 op_sel_hi:[1,0]
	v_pk_add_f32 v[200:201], v[200:201], 1.0 op_sel_hi:[1,0]
	v_pk_mul_f32 v[202:203], v[186:187], v[202:203]
	v_pk_mul_f32 v[200:201], v[184:185], v[200:201]
	ds_write_b128 v7, v[200:203] offset:57344
	s_waitcnt vmcnt(3)
	ds_write_b128 v165, v[220:223]
	s_waitcnt vmcnt(2)
	ds_write_b128 v165, v[224:227] offset:8192
	s_waitcnt vmcnt(1)
	ds_write_b128 v165, v[228:231] offset:16384
	s_waitcnt vmcnt(0)
	ds_write_b128 v165, v[232:235] offset:24576
	v_add_u32_e32 v6, 0x1800, v6
	v_add_u32_e32 v7, 0x18000, v7
	v_add_u32_e32 v8, 0x6000, v8

.LBB0_5877:
	s_or_b64 exec, exec, s[2:3]
	v_add_u32_e32 v4, s10, v0
	s_movk_i32 s2, 0xa00
	v_cmp_gt_i32_e32 vcc, s2, v4
	s_waitcnt lgkmcnt(0)
	s_barrier
	s_and_saveexec_b64 s[2:3], vcc
	s_cbranch_execz .LBB0_5882
	s_add_u32 s10, s0, 0x42000
	v_lshlrev_b32_e32 v1, 4, v0
	v_readlane_b32 s12, v252, 10
	v_lshlrev_b32_e32 v0, 2, v0
	s_addc_u32 s11, s1, 0
	v_lshl_add_u32 v5, s12, 10, v1
	v_lshl_add_u32 v6, s12, 8, v0
	s_mov_b64 s[12:13], 0
	v_mov_b32_e32 v1, 0
	s_movk_i32 s16, 0x7ff
	v_lshrrev_b32_e32 v164, 4, v4
	v_and_b32_e32 v0, 0x400, v6
	v_and_b32_e32 v7, 0x3f0, v5
	v_and_b32_e32 v164, 12, v164
	v_or3_b32 v164, v0, v7, v164
	v_lshlrev_b32_e32 v164, 2, v164
	s_mov_b64 s[98:99], s[10:11]
	global_load_dwordx4 v[168:171], v164, s[98:99]
	s_add_u32 s98, s10, 0xc000
	s_addc_u32 s99, s11, 0
	global_load_dwordx4 v[172:175], v164, s[98:99]
	s_add_u32 s98, s10, 0x18000
	s_addc_u32 s99, s11, 0
	global_load_dwordx4 v[176:179], v164, s[98:99]
	s_add_u32 s98, s10, 0x24000
	s_addc_u32 s99, s11, 0
	global_load_dwordx4 v[180:183], v164, s[98:99]
	global_load_dwordx4 v[184:187], v164, s[4:5]
	s_waitcnt vmcnt(4)
	ds_write_b128 v5, v[168:171]
	s_waitcnt vmcnt(3)
	ds_write_b128 v5, v[172:175] offset:8192
	s_waitcnt vmcnt(2)
	ds_write_b128 v5, v[176:179] offset:16384
	s_waitcnt vmcnt(1)
	ds_write_b128 v5, v[180:183] offset:24576
	s_waitcnt vmcnt(0)
	ds_write_b128 v5, v[184:187] offset:32768
